# QK^T LDS fragment reads software-pipelined 3 groups deep in the dilated, MoBA-own and gathered tile loops
# baseline (speedup 1.0000x reference)
; __device__ __forceinline__ void qkt(f32x16& p0, f32x16& p1, const f32x16& init, const char* Kt, int r32, int hi, const char* qf  ) {
;     p0 = init; p1 = init;
;     const char* kb[4];
; #pragma unroll
;     for (int dd = 0; dd < 4; ++dd) kb[dd] = Kt + KSWZ(r32, (dd * 16 + hi * 8) * 2);
; #pragma unroll
;     for (int d0 = 0; d0 < 8; ++d0) { const char* a = kb[d0 & 3] + (d0 >> 2) * 128;
;         bf16x8 b0 = *reinterpret_cast<const bf16x8*>(a);
;         bf16x8 b1 = *reinterpret_cast<const bf16x8*>(a + 32 * 256);
;         const bf16x8 q = *reinterpret_cast<const bf16x8*>(qf + d0 * 1024);
;         p0 = __builtin_amdgcn_mfma_f32_32x32x16_bf16(b0, q, p0, 0, 0, 0);
;         p1 = __builtin_amdgcn_mfma_f32_32x32x16_bf16(b1, q, p1, 0, 0, 0); }
; }
; template <int mode> __device__ __forceinline__ void attn_unit(const AttnArgs& A, const int b, const int h, const int sub, char* shm, const int wave_) {
;     ...
;         const int buf = t & 1; const int kb = __builtin_amdgcn_readfirstlane(TL[t]);
;         const bool more = (t + 1 < NT);
;         if (more) { const int k1 = __builtin_amdgcn_readfirstlane(TL[t + 1]); TDMA(k1, buf ^ 1); }
.LBB0_523:
	s_add_i32 s0, s29, -4
	v_mov_b32_e32 v0, s0
	ds_read2_b32 v[82:83], v0 offset1:1
	v_mov_b32_e32 v0, v126
	v_mov_b32_e32 v84, v125
	s_waitcnt lgkmcnt(0)
	v_readfirstlane_b32 s0, v83
	s_mul_i32 s31, s0, 0x3000
	s_mul_hi_i32 s30, s0, 0x3000
	s_add_u32 s0, s15, s31
	s_addc_u32 s1, s22, s30
	s_add_u32 s34, s23, s31
	s_addc_u32 s35, s27, s30
	s_and_b32 s30, s28, 0x4000
	s_xor_b32 s31, s30, 0x4000
	s_add_i32 s31, s2, s31
	s_add_i32 m0, s31, 0x8000
	v_mov_b32_e32 v83, v127
	global_load_lds_dwordx4 v84, s[0:1]
	s_mov_b32 m0, s31
	s_andn2_b64 vcc, exec, s[24:25]
	global_load_lds_dwordx4 v0, s[34:35]
	v_mov_b32_e32 v0, v128
	s_add_i32 m0, s31, 0x8400
	s_nop 0
	global_load_lds_dwordx4 v83, s[0:1]
	s_add_i32 m0, s31, 0x400
	v_readfirstlane_b32 s0, v82
	global_load_lds_dwordx4 v0, s[34:35]
	v_cndmask_b32_e64 v0, 0, 1, s[24:25]
	v_cmp_ne_u32_e64 s[44:45], 1, v0
	s_cbranch_vccnz .LBB0_522
	s_add_i32 s1, s30, 0
	v_add3_u32 v0, s1, v135, v130
	v_add3_u32 v144, s1, v134, v130
	v_add3_u32 v145, s1, v132, v130
	v_add3_u32 v146, s1, v131, v130
	v_cvt_f32_i32_e32 v136, s0
	ds_read_b128 v[208:211], v0 offset:32768
	ds_read_b128 v[212:215], v0 offset:40960
	ds_read_b128 v[216:219], v123
	ds_read_b128 v[220:223], v144 offset:32768
	ds_read_b128 v[224:227], v144 offset:40960
	ds_read_b128 v[228:231], v123 offset:1024
	ds_read_b128 v[232:235], v145 offset:32768
	ds_read_b128 v[236:239], v145 offset:40960
	ds_read_b128 v[240:243], v123 offset:2048
	s_waitcnt lgkmcnt(6)
	v_mfma_f32_32x32x16_bf16 v[82:97], v[208:211], v[216:219], v[66:81]
	v_mfma_f32_32x32x16_bf16 v[98:113], v[212:215], v[216:219], v[66:81]
	ds_read_b128 v[208:211], v146 offset:32768
	ds_read_b128 v[212:215], v146 offset:40960
	ds_read_b128 v[216:219], v123 offset:3072
	s_waitcnt lgkmcnt(6)
	v_mfma_f32_32x32x16_bf16 v[82:97], v[220:223], v[228:231], v[82:97]
	v_mfma_f32_32x32x16_bf16 v[98:113], v[224:227], v[228:231], v[98:113]
	ds_read_b128 v[220:223], v0 offset:32896
	ds_read_b128 v[224:227], v0 offset:41088
	ds_read_b128 v[228:231], v123 offset:4096
	s_waitcnt lgkmcnt(6)
	v_mfma_f32_32x32x16_bf16 v[82:97], v[232:235], v[240:243], v[82:97]
	v_mfma_f32_32x32x16_bf16 v[98:113], v[236:239], v[240:243], v[98:113]
	ds_read_b128 v[232:235], v144 offset:32896
	ds_read_b128 v[236:239], v144 offset:41088
	ds_read_b128 v[240:243], v123 offset:5120
	s_waitcnt lgkmcnt(6)
	v_mfma_f32_32x32x16_bf16 v[82:97], v[208:211], v[216:219], v[82:97]
	v_mfma_f32_32x32x16_bf16 v[98:113], v[212:215], v[216:219], v[98:113]
	ds_read_b128 v[208:211], v145 offset:32896
	ds_read_b128 v[212:215], v145 offset:41088
	ds_read_b128 v[216:219], v123 offset:6144
	s_waitcnt lgkmcnt(6)
	v_mfma_f32_32x32x16_bf16 v[82:97], v[220:223], v[228:231], v[82:97]
	v_mfma_f32_32x32x16_bf16 v[98:113], v[224:227], v[228:231], v[98:113]
	ds_read_b128 v[220:223], v146 offset:41088
	ds_read_b128 v[224:227], v146 offset:32896
	ds_read_b128 v[228:231], v123 offset:7168
	s_waitcnt lgkmcnt(6)
	v_mfma_f32_32x32x16_bf16 v[82:97], v[232:235], v[240:243], v[82:97]
	v_mfma_f32_32x32x16_bf16 v[98:113], v[236:239], v[240:243], v[98:113]
	s_waitcnt lgkmcnt(3)
	v_mfma_f32_32x32x16_bf16 v[82:97], v[208:211], v[216:219], v[82:97]
	v_mfma_f32_32x32x16_bf16 v[98:113], v[212:215], v[216:219], v[98:113]
	s_waitcnt lgkmcnt(0)
; template <int mode> __device__ __forceinline__ void attn_unit(const AttnArgs& A, const int b, const int h, const int sub, char* shm, const int wave_) {
;     ...
;                 const float tb = sl * (float)kb;
;                 float pm0 = p0[0], pm1 = p1[0];
; #pragma unroll
;                 for (int r = 1; r < 16; ++r) { pm0 = fmaxf(pm0, p0[r]); pm1 = fmaxf(pm1, p1[r]); }
;                 float pmax = fmaxf(pm0, pm1 + sl32);
;                 { auto rr = __builtin_amdgcn_permlane32_swap(__float_as_uint(pmax), __float_as_uint(pmax), false, false); pmax = fmaxf(__uint_as_float(rr[0]), __uint_as_float(rr[1])); }
;                 pmax = rowok ? pmax : NEG;
;                 const float m_loc = m_reg - tb;
;                 const float mn = fmaxf(m_loc, pmax); const float alpha = __builtin_amdgcn_exp2f(m_loc - mn); m_reg = mn + tb;
;                 const float ref0 = rowok ? mn : __builtin_inff(), ref1 = ref0 - sl32;
;                 float ps = 0.f;
; #pragma unroll
;                 for (int r = 0; r < 16; ++r) { p0[r] = __builtin_amdgcn_exp2f(p0[r] - ref0); p1[r] = __builtin_amdgcn_exp2f(p1[r] - ref1); ps += p0[r] + p1[r]; }
;                 { auto rr = __builtin_amdgcn_permlane32_swap(__float_as_uint(ps), __float_as_uint(ps), false, false); ps = __uint_as_float(rr[0]) + __uint_as_float(rr[1]); }
;                 l_reg = l_reg * alpha + ps;
;                 pack_p(p0, p1, pa0, pa1, pa2, pa3);
;                 if (__any(alpha < 1.f)) { if (hi == 0) al_l[r32] = alpha; asm volatile("s_waitcnt lgkmcnt(0)" ::: "memory");
	v_mfma_f32_32x32x16_bf16 v[98:113], v[220:223], v[228:231], v[98:113]
	v_mfma_f32_32x32x16_bf16 v[82:97], v[224:227], v[228:231], v[82:97]
	s_nop 1
	s_nop 9
	v_max_f32_e32 v0, v99, v99
	v_max_f32_e32 v137, v98, v98
	v_max_f32_e32 v0, v137, v0
	v_max3_f32 v0, v0, v100, v101
	v_max3_f32 v0, v0, v102, v103
	v_max3_f32 v0, v0, v104, v105
	v_max3_f32 v0, v0, v106, v107
	v_max3_f32 v137, v82, v83, v84
	v_max3_f32 v137, v137, v85, v86
	v_max3_f32 v137, v137, v87, v88
	v_max3_f32 v137, v137, v89, v90
	v_max3_f32 v0, v0, v108, v109
	v_max3_f32 v137, v137, v91, v92
	v_max3_f32 v0, v0, v110, v111
	v_max3_f32 v137, v137, v93, v94
	v_max3_f32 v0, v0, v112, v113
	v_max3_f32 v137, v137, v95, v96
	v_add_f32_e32 v0, v129, v0
	v_max3_f32 v0, v137, v97, v0
	v_mov_b32_e32 v137, v0
	s_nop 1
	v_permlane32_swap_b32_e32 v0, v137
	v_max_f32_e32 v137, v137, v137
	v_max_f32_e32 v0, v0, v0
	v_max_f32_e32 v0, v0, v137
	v_cndmask_b32_e64 v0, v206, v0, s[40:41]
	v_fma_f32 v137, -v118, v136, v116
	v_max_f32_e32 v116, v137, v0
	v_mov_b32_e32 v0, 0x7f800000
	v_cndmask_b32_e64 v142, v0, v116, s[40:41]
	v_sub_f32_e32 v143, v142, v129
	v_sub_f32_e32 v0, v82, v142
	v_exp_f32_e32 v144, v0
	v_sub_f32_e32 v0, v98, v143
	v_exp_f32_e32 v145, v0
	v_sub_f32_e32 v0, v83, v142
	v_exp_f32_e32 v82, v0
	v_sub_f32_e32 v0, v99, v143
	v_exp_f32_e32 v0, v0
	v_add_f32_e32 v83, v144, v145
	v_pk_add_f32 v[98:99], v[82:83], v[0:1]
	v_sub_f32_e32 v83, v84, v142
	v_sub_f32_e32 v84, v100, v143
	v_pk_add_f32 v[138:139], v[98:99], v[98:99] op_sel_hi:[0,1]
	v_exp_f32_e32 v83, v83
	v_exp_f32_e32 v146, v84
	v_sub_f32_e32 v84, v85, v142
	v_sub_f32_e32 v85, v101, v143
	v_exp_f32_e32 v84, v84
	v_exp_f32_e32 v138, v85
	v_add_f32_e32 v85, v83, v146
	v_cvt_pk_bf16_f32 v82, v144, v82
	v_cvt_pk_bf16_f32 v83, v83, v84
	v_pk_add_f32 v[98:99], v[84:85], v[138:139]
	v_sub_f32_e32 v85, v86, v142
	v_sub_f32_e32 v86, v102, v143
	v_pk_add_f32 v[100:101], v[98:99], v[98:99] op_sel_hi:[0,1]
	v_exp_f32_e32 v85, v85
	v_exp_f32_e32 v139, v86
	v_sub_f32_e32 v86, v87, v142
	v_sub_f32_e32 v87, v103, v143
	v_exp_f32_e32 v86, v86
	v_exp_f32_e32 v100, v87
	v_add_f32_e32 v87, v85, v139
	v_cvt_pk_bf16_f32 v84, v85, v86
	v_pk_add_f32 v[98:99], v[86:87], v[100:101]
	v_sub_f32_e32 v87, v88, v142
	v_sub_f32_e32 v88, v104, v143
	v_pk_add_f32 v[140:141], v[98:99], v[98:99] op_sel_hi:[0,1]
	v_exp_f32_e32 v87, v87
	v_exp_f32_e32 v101, v88
	v_sub_f32_e32 v88, v89, v142
	v_sub_f32_e32 v89, v105, v143
	v_exp_f32_e32 v88, v88
	v_exp_f32_e32 v140, v89
	v_add_f32_e32 v89, v87, v101
	v_cvt_pk_bf16_f32 v85, v87, v88
	v_permlane32_swap_b32_e32 v82, v84
	v_pk_add_f32 v[98:99], v[88:89], v[140:141]
	v_sub_f32_e32 v89, v90, v142
	v_sub_f32_e32 v90, v106, v143
	v_pk_add_f32 v[104:105], v[98:99], v[98:99] op_sel_hi:[0,1]
	v_exp_f32_e32 v89, v89
	v_exp_f32_e32 v103, v90
	v_sub_f32_e32 v90, v91, v142
	v_sub_f32_e32 v91, v107, v143
	v_exp_f32_e32 v90, v90
	v_exp_f32_e32 v104, v91
	v_add_f32_e32 v91, v89, v103
	v_cvt_pk_bf16_f32 v86, v89, v90
	v_permlane32_swap_b32_e32 v83, v85
	v_pk_add_f32 v[98:99], v[90:91], v[104:105]
	v_sub_f32_e32 v91, v92, v142
	v_sub_f32_e32 v92, v108, v143
	v_pk_add_f32 v[106:107], v[98:99], v[98:99] op_sel_hi:[0,1]
	v_exp_f32_e32 v91, v91
	v_exp_f32_e32 v105, v92
	v_sub_f32_e32 v92, v93, v142
	v_sub_f32_e32 v93, v109, v143
	v_exp_f32_e32 v92, v92
	v_exp_f32_e32 v106, v93
	v_add_f32_e32 v93, v91, v105
	v_cvt_pk_bf16_f32 v87, v91, v92
	v_pk_add_f32 v[98:99], v[92:93], v[106:107]
	v_sub_f32_e32 v93, v94, v142
	v_sub_f32_e32 v94, v110, v143
	v_pk_add_f32 v[108:109], v[98:99], v[98:99] op_sel_hi:[0,1]
	v_exp_f32_e32 v93, v93
	v_exp_f32_e32 v107, v94
	v_sub_f32_e32 v94, v95, v142
	v_sub_f32_e32 v95, v111, v143
	v_exp_f32_e32 v94, v94
	v_exp_f32_e32 v108, v95
	v_add_f32_e32 v95, v93, v107
	v_cvt_pk_bf16_f32 v88, v93, v94
	v_pk_add_f32 v[98:99], v[94:95], v[108:109]
	v_sub_f32_e32 v95, v96, v142
	v_sub_f32_e32 v96, v112, v143
	v_pk_add_f32 v[110:111], v[98:99], v[98:99] op_sel_hi:[0,1]
	v_exp_f32_e32 v95, v95
	v_exp_f32_e32 v109, v96
	v_sub_f32_e32 v96, v97, v142
	v_sub_f32_e32 v97, v113, v143
	v_exp_f32_e32 v96, v96
	v_exp_f32_e32 v110, v97
	v_sub_f32_e32 v97, v137, v116
	v_exp_f32_e32 v102, v97
	v_add_f32_e32 v97, v95, v109
	v_pk_add_f32 v[98:99], v[96:97], v[110:111]
	v_cvt_pk_bf16_f32 v89, v95, v96
	v_cvt_pk_bf16_f32 v90, v145, v0
	v_cvt_pk_bf16_f32 v91, v146, v138
	v_cvt_pk_bf16_f32 v92, v139, v100
	v_cvt_pk_bf16_f32 v93, v101, v140
	s_nop 0
	v_pk_add_f32 v[98:99], v[98:99], v[98:99] op_sel:[0,1] op_sel_hi:[1,0]
	v_cvt_pk_bf16_f32 v94, v103, v104
	v_cvt_pk_bf16_f32 v95, v105, v106
	v_cvt_pk_bf16_f32 v96, v107, v108
	v_cvt_pk_bf16_f32 v97, v109, v110
	v_permlane32_swap_b32_e32 v86, v88
	v_mov_b32_e32 v99, v98
	s_nop 1
	v_permlane32_swap_b32_e32 v98, v99
	v_permlane32_swap_b32_e32 v87, v89
	v_permlane32_swap_b32_e32 v90, v92
	v_permlane32_swap_b32_e32 v91, v93
	v_permlane32_swap_b32_e32 v94, v96
	v_permlane32_swap_b32_e32 v95, v97
	v_cmp_gt_f32_e32 vcc, 1.0, v102
	s_cbranch_vccz .LBB0_521
	s_and_saveexec_b64 s[0:1], s[42:43]
	s_cbranch_execz .LBB0_520
	ds_write_b32 v115, v102 offset:128
	s_branch .LBB0_520

; __device__ __forceinline__ void qkt(f32x16& p0, f32x16& p1, const f32x16& init, const char* Kt, int r32, int hi, const char* qf  ) {
;     p0 = init; p1 = init;
;     const char* kb[4];
; #pragma unroll
;     for (int dd = 0; dd < 4; ++dd) kb[dd] = Kt + KSWZ(r32, (dd * 16 + hi * 8) * 2);
; #pragma unroll
;     for (int d0 = 0; d0 < 8; ++d0) { const char* a = kb[d0 & 3] + (d0 >> 2) * 128;
;         bf16x8 b0 = *reinterpret_cast<const bf16x8*>(a);
;         bf16x8 b1 = *reinterpret_cast<const bf16x8*>(a + 32 * 256);
;         const bf16x8 q = *reinterpret_cast<const bf16x8*>(qf + d0 * 1024);
;         p0 = __builtin_amdgcn_mfma_f32_32x32x16_bf16(b0, q, p0, 0, 0, 0);
;         p1 = __builtin_amdgcn_mfma_f32_32x32x16_bf16(b1, q, p1, 0, 0, 0); }
; }
; template <int mode> __device__ __forceinline__ void attn_unit(const AttnArgs& A, const int b, const int h, const int sub, char* shm, const int wave_) {
;     ...
;                 } else if (mode == 1) {
;                     if (kb + 63 > qw0) {
; #pragma unroll
;                         for (int r = 0; r < 16; ++r) { const int c = (r & 3) + 8 * (r >> 2);
;                             p0[r] = (dq - c >= 0) ? p0[r] : NEG; p1[r] = (dq - c - 32 >= 0) ? p1[r] : NEG; } }
.LBB0_844:
	s_add_i32 s0, s30, -4
	v_mov_b32_e32 v0, s0
	ds_read2_b32 v[82:83], v0 offset1:1
	v_mov_b32_e32 v0, v152
	v_mov_b32_e32 v84, v150
	s_waitcnt lgkmcnt(0)
	v_readfirstlane_b32 s0, v83
	s_mul_i32 s35, s0, 0x3000
	s_mul_hi_i32 s31, s0, 0x3000
	s_add_u32 s0, s14, s35
	s_addc_u32 s1, s15, s31
	s_add_u32 s38, s25, s35
	s_addc_u32 s39, s27, s31
	s_and_b32 s31, s22, 0x4000
	s_xor_b32 s35, s31, 0x4000
	s_add_i32 s35, s2, s35
	s_add_i32 m0, s35, 0x8000
	v_mov_b32_e32 v83, v154
	global_load_lds_dwordx4 v84, s[0:1]
	s_mov_b32 m0, s35
	s_nop 0
	global_load_lds_dwordx4 v0, s[38:39]
	v_mov_b32_e32 v0, v156
	s_add_i32 m0, s35, 0x8400
	s_nop 0
	global_load_lds_dwordx4 v83, s[0:1]
	s_add_i32 m0, s35, 0x400
	v_readfirstlane_b32 s0, v82
	global_load_lds_dwordx4 v0, s[38:39]
	s_cmp_gt_i32 s0, s23
	s_cbranch_scc1 .LBB0_843
	s_add_i32 s1, s31, 0
	v_add3_u32 v0, s1, v173, v161
	v_add3_u32 v174, s1, v172, v161
	v_add3_u32 v175, s1, v171, v161
	v_add3_u32 v176, s1, v170, v161
	s_cmp_le_i32 s0, s29
	ds_read_b128 v[208:211], v0 offset:32768
	ds_read_b128 v[212:215], v0 offset:40960
	ds_read_b128 v[216:219], v140
	ds_read_b128 v[220:223], v174 offset:32768
	ds_read_b128 v[224:227], v174 offset:40960
	ds_read_b128 v[228:231], v140 offset:1024
	ds_read_b128 v[232:235], v175 offset:32768
	ds_read_b128 v[236:239], v175 offset:40960
	ds_read_b128 v[240:243], v140 offset:2048
	s_waitcnt lgkmcnt(6)
	v_mfma_f32_32x32x16_bf16 v[82:97], v[208:211], v[216:219], v[66:81]
	v_mfma_f32_32x32x16_bf16 v[98:113], v[212:215], v[216:219], v[66:81]
	ds_read_b128 v[208:211], v176 offset:32768
	ds_read_b128 v[212:215], v176 offset:40960
	ds_read_b128 v[216:219], v140 offset:3072
	s_waitcnt lgkmcnt(6)
	v_mfma_f32_32x32x16_bf16 v[82:97], v[220:223], v[228:231], v[82:97]
	v_mfma_f32_32x32x16_bf16 v[98:113], v[224:227], v[228:231], v[98:113]
	ds_read_b128 v[220:223], v0 offset:32896
	ds_read_b128 v[224:227], v0 offset:41088
	ds_read_b128 v[228:231], v140 offset:4096
	s_waitcnt lgkmcnt(6)
	v_mfma_f32_32x32x16_bf16 v[82:97], v[232:235], v[240:243], v[82:97]
	v_mfma_f32_32x32x16_bf16 v[98:113], v[236:239], v[240:243], v[98:113]
	ds_read_b128 v[232:235], v174 offset:32896
	ds_read_b128 v[236:239], v174 offset:41088
	ds_read_b128 v[240:243], v140 offset:5120
	s_waitcnt lgkmcnt(6)
	v_mfma_f32_32x32x16_bf16 v[82:97], v[208:211], v[216:219], v[82:97]
	v_mfma_f32_32x32x16_bf16 v[98:113], v[212:215], v[216:219], v[98:113]
	ds_read_b128 v[208:211], v175 offset:32896
	ds_read_b128 v[212:215], v175 offset:41088
	ds_read_b128 v[216:219], v140 offset:6144
	s_waitcnt lgkmcnt(6)
	v_mfma_f32_32x32x16_bf16 v[82:97], v[220:223], v[228:231], v[82:97]
	v_mfma_f32_32x32x16_bf16 v[98:113], v[224:227], v[228:231], v[98:113]
	ds_read_b128 v[220:223], v176 offset:32896
	ds_read_b128 v[224:227], v176 offset:41088
	ds_read_b128 v[228:231], v140 offset:7168
	s_waitcnt lgkmcnt(6)
	v_mfma_f32_32x32x16_bf16 v[82:97], v[232:235], v[240:243], v[82:97]
	v_mfma_f32_32x32x16_bf16 v[98:113], v[236:239], v[240:243], v[98:113]
	s_waitcnt lgkmcnt(3)
	v_mfma_f32_32x32x16_bf16 v[82:97], v[208:211], v[216:219], v[82:97]
	v_mfma_f32_32x32x16_bf16 v[98:113], v[212:215], v[216:219], v[98:113]
	s_waitcnt lgkmcnt(0)
	v_mfma_f32_32x32x16_bf16 v[82:97], v[220:223], v[228:231], v[82:97]
	v_mfma_f32_32x32x16_bf16 v[98:113], v[224:227], v[228:231], v[98:113]
	s_nop 1
	s_cbranch_scc1 .LBB0_847
	v_add_u32_e32 v0, s0, v142
	v_sub_u32_e32 v162, v139, v0
	v_cmp_lt_i32_e32 vcc, -1, v162
	s_nop 4
	v_cndmask_b32_e32 v82, v206, v82, vcc
	v_cmp_lt_i32_e32 vcc, 31, v162
	v_xad_u32 v162, v0, -1, v139
	s_nop 0
	v_cndmask_b32_e32 v98, v206, v98, vcc
	v_cmp_lt_i32_e32 vcc, -1, v162
	s_nop 1
	v_cndmask_b32_e32 v83, v206, v83, vcc
	v_cmp_lt_i32_e32 vcc, 31, v162
	v_sub_u32_e32 v162, v160, v0
	s_nop 0
	v_cndmask_b32_e32 v99, v206, v99, vcc
	v_cmp_lt_i32_e32 vcc, -1, v162
	s_nop 1
	v_cndmask_b32_e32 v84, v206, v84, vcc
	v_cmp_lt_i32_e32 vcc, 31, v162
	v_sub_u32_e32 v162, v159, v0
	s_nop 0
	v_cndmask_b32_e32 v100, v206, v100, vcc
	v_cmp_lt_i32_e32 vcc, -1, v162
	s_nop 1
	v_cndmask_b32_e32 v85, v206, v85, vcc
	v_cmp_lt_i32_e32 vcc, 31, v162
	v_sub_u32_e32 v162, v158, v0
	s_nop 0
	v_cndmask_b32_e32 v101, v206, v101, vcc
	v_cmp_lt_i32_e32 vcc, -1, v162
	s_nop 1
	v_cndmask_b32_e32 v86, v206, v86, vcc
	v_cmp_lt_i32_e32 vcc, 31, v162
	v_sub_u32_e32 v162, v157, v0
	s_nop 0
	v_cndmask_b32_e32 v102, v206, v102, vcc
	v_cmp_lt_i32_e32 vcc, -1, v162
	s_nop 1
	v_cndmask_b32_e32 v87, v206, v87, vcc
	v_cmp_lt_i32_e32 vcc, 31, v162
	v_sub_u32_e32 v162, v155, v0
	s_nop 0
	v_cndmask_b32_e32 v103, v206, v103, vcc
	v_cmp_lt_i32_e32 vcc, -1, v162
	s_nop 1
	v_cndmask_b32_e32 v88, v206, v88, vcc
	v_cmp_lt_i32_e32 vcc, 31, v162
	v_sub_u32_e32 v162, v153, v0
	s_nop 0
	v_cndmask_b32_e32 v104, v206, v104, vcc
	v_cmp_lt_i32_e32 vcc, -1, v162
	s_nop 1
	v_cndmask_b32_e32 v89, v206, v89, vcc
	v_cmp_lt_i32_e32 vcc, 31, v162
	v_sub_u32_e32 v162, v151, v0
	s_nop 0
	v_cndmask_b32_e32 v105, v206, v105, vcc
	v_cmp_lt_i32_e32 vcc, -1, v162
	s_nop 1
	v_cndmask_b32_e32 v90, v206, v90, vcc
	v_cmp_lt_i32_e32 vcc, 31, v162
	v_sub_u32_e32 v162, v149, v0
	s_nop 0
	v_cndmask_b32_e32 v106, v206, v106, vcc
	v_cmp_lt_i32_e32 vcc, -1, v162
	s_nop 1
	v_cndmask_b32_e32 v91, v206, v91, vcc
	v_cmp_lt_i32_e32 vcc, 31, v162
	v_sub_u32_e32 v162, v148, v0
	s_nop 0
	v_cndmask_b32_e32 v107, v206, v107, vcc
	v_cmp_lt_i32_e32 vcc, -1, v162
	s_nop 1
	v_cndmask_b32_e32 v92, v206, v92, vcc
	v_cmp_lt_i32_e32 vcc, 31, v162
	v_sub_u32_e32 v162, v147, v0
	s_nop 0
	v_cndmask_b32_e32 v108, v206, v108, vcc
	v_cmp_lt_i32_e32 vcc, -1, v162
	s_nop 1
	v_cndmask_b32_e32 v93, v206, v93, vcc
	v_cmp_lt_i32_e32 vcc, 31, v162
	v_sub_u32_e32 v162, v146, v0
	s_nop 0
	v_cndmask_b32_e32 v109, v206, v109, vcc
	v_cmp_lt_i32_e32 vcc, -1, v162
	s_nop 1
	v_cndmask_b32_e32 v94, v206, v94, vcc
	v_cmp_lt_i32_e32 vcc, 31, v162
	v_sub_u32_e32 v162, v145, v0
	s_nop 0
	v_cndmask_b32_e32 v110, v206, v110, vcc
	v_cmp_lt_i32_e32 vcc, -1, v162
	s_nop 1
	v_cndmask_b32_e32 v95, v206, v95, vcc
	v_cmp_lt_i32_e32 vcc, 31, v162
	v_sub_u32_e32 v162, v144, v0
	v_sub_u32_e32 v0, v143, v0
	v_cndmask_b32_e32 v111, v206, v111, vcc
	v_cmp_lt_i32_e32 vcc, -1, v162
	s_nop 1
	v_cndmask_b32_e32 v96, v206, v96, vcc
	v_cmp_lt_i32_e32 vcc, 31, v162
	s_nop 1
	v_cndmask_b32_e32 v112, v206, v112, vcc
	v_cmp_lt_i32_e32 vcc, -1, v0
	s_nop 1
	v_cndmask_b32_e32 v97, v206, v97, vcc
	v_cmp_lt_i32_e32 vcc, 31, v0
	s_nop 1
	v_cndmask_b32_e32 v113, v206, v113, vcc

; __device__ __forceinline__ void qkt(f32x16& p0, f32x16& p1, const f32x16& init, const char* Kt, int r32, int hi, const char* qf  ) {
;     p0 = init; p1 = init;
;     const char* kb[4];
; #pragma unroll
;     for (int dd = 0; dd < 4; ++dd) kb[dd] = Kt + KSWZ(r32, (dd * 16 + hi * 8) * 2);
; #pragma unroll
;     for (int d0 = 0; d0 < 8; ++d0) { const char* a = kb[d0 & 3] + (d0 >> 2) * 128;
;         bf16x8 b0 = *reinterpret_cast<const bf16x8*>(a);
;         bf16x8 b1 = *reinterpret_cast<const bf16x8*>(a + 32 * 256);
;         const bf16x8 q = *reinterpret_cast<const bf16x8*>(qf + d0 * 1024);
;         p0 = __builtin_amdgcn_mfma_f32_32x32x16_bf16(b0, q, p0, 0, 0, 0);
;         p1 = __builtin_amdgcn_mfma_f32_32x32x16_bf16(b1, q, p1, 0, 0, 0); }
; }
; template <int mode> __device__ __forceinline__ void attn_unit(const AttnArgs& A, const int b, const int h, const int sub, char* shm, const int wave_) {
;     ...
;                 if (mode == 0) {
;                     if (!((kb + 63 <= qw0) && (qw0 + 31 - kb <= 128))) {
; #pragma unroll
;                         for (int r = 0; r < 16; ++r) { const int c = (r & 3) + 8 * (r >> 2);
;                             p0[r] = ((unsigned)(dq - c) <= 128u) ? p0[r] : NEG; p1[r] = ((unsigned)(dq - c - 32) <= 128u) ? p1[r] : NEG; } }
.LBB0_879:
	s_cmp_le_i32 s42, s30
	s_cselect_b64 s[14:15], -1, 0
	s_add_i32 s0, s42, 63
	s_cmp_ge_i32 s0, s31
	s_cselect_b64 s[44:45], -1, 0
	s_and_b64 s[14:15], s[14:15], s[44:45]
	s_andn2_b64 vcc, exec, s[14:15]
	s_cbranch_vccnz .LBB0_876
	s_lshl_b32 s14, s43, 14
	s_add_i32 s1, s14, 0
	v_add3_u32 v0, s1, v160, v159
	v_add3_u32 v10, s1, v161, v159
	v_add3_u32 v11, s1, v170, v159
	v_add3_u32 v12, s1, v171, v159
	s_cmp_le_i32 s0, s22
	s_cselect_b64 s[0:1], -1, 0
	s_cmp_gt_i32 s42, s35
	s_cselect_b64 s[44:45], -1, 0
	s_and_b64 s[0:1], s[0:1], s[44:45]
	s_and_b64 vcc, exec, s[0:1]
	ds_read_b128 v[208:211], v0 offset:32768
	ds_read_b128 v[212:215], v0 offset:40960
	ds_read_b128 v[216:219], v156
	ds_read_b128 v[220:223], v10 offset:32768
	ds_read_b128 v[224:227], v10 offset:40960
	ds_read_b128 v[228:231], v156 offset:1024
	ds_read_b128 v[232:235], v11 offset:32768
	ds_read_b128 v[236:239], v11 offset:40960
	ds_read_b128 v[240:243], v156 offset:2048
	s_waitcnt lgkmcnt(6)
	v_mfma_f32_32x32x16_bf16 v[96:111], v[208:211], v[216:219], v[80:95]
	v_mfma_f32_32x32x16_bf16 v[112:127], v[212:215], v[216:219], v[80:95]
	ds_read_b128 v[208:211], v12 offset:32768
	ds_read_b128 v[212:215], v12 offset:40960
	ds_read_b128 v[216:219], v156 offset:3072
	s_waitcnt lgkmcnt(6)
	v_mfma_f32_32x32x16_bf16 v[96:111], v[220:223], v[228:231], v[96:111]
	v_mfma_f32_32x32x16_bf16 v[112:127], v[224:227], v[228:231], v[112:127]
	ds_read_b128 v[220:223], v0 offset:32896
	ds_read_b128 v[224:227], v0 offset:41088
	ds_read_b128 v[228:231], v156 offset:4096
	s_waitcnt lgkmcnt(6)
	v_mfma_f32_32x32x16_bf16 v[96:111], v[232:235], v[240:243], v[96:111]
	v_mfma_f32_32x32x16_bf16 v[112:127], v[236:239], v[240:243], v[112:127]
	ds_read_b128 v[232:235], v10 offset:32896
	ds_read_b128 v[236:239], v10 offset:41088
	ds_read_b128 v[240:243], v156 offset:5120
	s_waitcnt lgkmcnt(6)
	v_mfma_f32_32x32x16_bf16 v[96:111], v[208:211], v[216:219], v[96:111]
	v_mfma_f32_32x32x16_bf16 v[112:127], v[212:215], v[216:219], v[112:127]
	ds_read_b128 v[208:211], v11 offset:32896
	ds_read_b128 v[212:215], v11 offset:41088
	ds_read_b128 v[216:219], v156 offset:6144
	s_waitcnt lgkmcnt(6)
	v_mfma_f32_32x32x16_bf16 v[96:111], v[220:223], v[228:231], v[96:111]
	v_mfma_f32_32x32x16_bf16 v[112:127], v[224:227], v[228:231], v[112:127]
	ds_read_b128 v[220:223], v12 offset:32896
	ds_read_b128 v[224:227], v12 offset:41088
	ds_read_b128 v[228:231], v156 offset:7168
	s_waitcnt lgkmcnt(6)
	v_mfma_f32_32x32x16_bf16 v[96:111], v[232:235], v[240:243], v[96:111]
	v_mfma_f32_32x32x16_bf16 v[112:127], v[236:239], v[240:243], v[112:127]
	s_waitcnt lgkmcnt(3)
	v_mfma_f32_32x32x16_bf16 v[96:111], v[208:211], v[216:219], v[96:111]
	v_mfma_f32_32x32x16_bf16 v[112:127], v[212:215], v[216:219], v[112:127]
	s_waitcnt lgkmcnt(0)
	v_mfma_f32_32x32x16_bf16 v[96:111], v[220:223], v[228:231], v[96:111]
	v_mfma_f32_32x32x16_bf16 v[112:127], v[224:227], v[228:231], v[112:127]
	s_nop 1
	s_cbranch_vccnz .LBB0_882
	v_add_u32_e32 v0, s42, v155
	v_sub_u32_e32 v2, v147, v0
	s_movk_i32 s0, 0x81
	v_cmp_gt_u32_e32 vcc, s0, v2
	v_subrev_u32_e32 v2, 32, v2
	s_nop 2
	v_cndmask_b32_e32 v96, v206, v96, vcc
	v_cmp_gt_u32_e32 vcc, s0, v2
	v_xad_u32 v2, v0, -1, v147
	s_nop 0
	v_cndmask_b32_e32 v112, v206, v112, vcc
	v_cmp_gt_u32_e32 vcc, s0, v2
	v_subrev_u32_e32 v2, 32, v2
	s_nop 0
	v_cndmask_b32_e32 v97, v206, v97, vcc
	v_cmp_gt_u32_e32 vcc, s0, v2
	v_sub_u32_e32 v2, v173, v0
	s_nop 0
	v_cndmask_b32_e32 v113, v206, v113, vcc
	v_cmp_gt_u32_e32 vcc, s0, v2
	v_subrev_u32_e32 v2, 32, v2
	s_nop 0
	v_cndmask_b32_e32 v98, v206, v98, vcc
	v_cmp_gt_u32_e32 vcc, s0, v2
	v_sub_u32_e32 v2, v174, v0
	s_nop 0
	v_cndmask_b32_e32 v114, v206, v114, vcc
	v_cmp_gt_u32_e32 vcc, s0, v2
	v_subrev_u32_e32 v2, 32, v2
	s_nop 0
	v_cndmask_b32_e32 v99, v206, v99, vcc
	v_cmp_gt_u32_e32 vcc, s0, v2
	v_sub_u32_e32 v2, v175, v0
	s_nop 0
	v_cndmask_b32_e32 v115, v206, v115, vcc
	v_cmp_gt_u32_e32 vcc, s0, v2
	v_subrev_u32_e32 v2, 32, v2
	s_nop 0
	v_cndmask_b32_e32 v100, v206, v100, vcc
	v_cmp_gt_u32_e32 vcc, s0, v2
	v_sub_u32_e32 v2, v176, v0
	s_nop 0
	v_cndmask_b32_e32 v116, v206, v116, vcc
	v_cmp_gt_u32_e32 vcc, s0, v2
	v_subrev_u32_e32 v2, 32, v2
	s_nop 0
	v_cndmask_b32_e32 v101, v206, v101, vcc
	v_cmp_gt_u32_e32 vcc, s0, v2
	v_sub_u32_e32 v2, v177, v0
	s_nop 0
	v_cndmask_b32_e32 v117, v206, v117, vcc
	v_cmp_gt_u32_e32 vcc, s0, v2
	v_subrev_u32_e32 v2, 32, v2
	s_nop 0
	v_cndmask_b32_e32 v102, v206, v102, vcc
	v_cmp_gt_u32_e32 vcc, s0, v2
	v_sub_u32_e32 v2, v178, v0
	s_nop 0
	v_cndmask_b32_e32 v118, v206, v118, vcc
	v_cmp_gt_u32_e32 vcc, s0, v2
	v_subrev_u32_e32 v2, 32, v2
	s_nop 0
	v_cndmask_b32_e32 v103, v206, v103, vcc
	v_cmp_gt_u32_e32 vcc, s0, v2
	v_sub_u32_e32 v2, v179, v0
	s_nop 0
	v_cndmask_b32_e32 v119, v206, v119, vcc
	v_cmp_gt_u32_e32 vcc, s0, v2
	v_subrev_u32_e32 v2, 32, v2
	s_nop 0
	v_cndmask_b32_e32 v104, v206, v104, vcc
	v_cmp_gt_u32_e32 vcc, s0, v2
	v_sub_u32_e32 v2, v180, v0
	s_nop 0
	v_cndmask_b32_e32 v120, v206, v120, vcc
	v_cmp_gt_u32_e32 vcc, s0, v2
	v_subrev_u32_e32 v2, 32, v2
	s_nop 0
	v_cndmask_b32_e32 v105, v206, v105, vcc
	v_cmp_gt_u32_e32 vcc, s0, v2
	v_sub_u32_e32 v2, v181, v0
	s_nop 0
	v_cndmask_b32_e32 v121, v206, v121, vcc
	v_cmp_gt_u32_e32 vcc, s0, v2
	v_subrev_u32_e32 v2, 32, v2
	s_nop 0
	v_cndmask_b32_e32 v106, v206, v106, vcc
	v_cmp_gt_u32_e32 vcc, s0, v2
	v_sub_u32_e32 v2, v182, v0
	s_nop 0
	v_cndmask_b32_e32 v122, v206, v122, vcc
	v_cmp_gt_u32_e32 vcc, s0, v2
	v_subrev_u32_e32 v2, 32, v2
	s_nop 0
	v_cndmask_b32_e32 v107, v206, v107, vcc
	v_cmp_gt_u32_e32 vcc, s0, v2
	v_sub_u32_e32 v2, v183, v0
	s_nop 0
	v_cndmask_b32_e32 v123, v206, v123, vcc
	v_cmp_gt_u32_e32 vcc, s0, v2
	v_subrev_u32_e32 v2, 32, v2
	s_nop 0
	v_cndmask_b32_e32 v108, v206, v108, vcc
	v_cmp_gt_u32_e32 vcc, s0, v2
	v_sub_u32_e32 v2, v184, v0
	s_nop 0
	v_cndmask_b32_e32 v124, v206, v124, vcc
	v_cmp_gt_u32_e32 vcc, s0, v2
	v_subrev_u32_e32 v2, 32, v2
	s_nop 0
	v_cndmask_b32_e32 v109, v206, v109, vcc
	v_cmp_gt_u32_e32 vcc, s0, v2
	v_sub_u32_e32 v2, v185, v0
	v_sub_u32_e32 v0, v186, v0
	v_cndmask_b32_e32 v125, v206, v125, vcc
	v_cmp_gt_u32_e32 vcc, s0, v2
	v_subrev_u32_e32 v2, 32, v2
	s_nop 0
	v_cndmask_b32_e32 v110, v206, v110, vcc
	v_cmp_gt_u32_e32 vcc, s0, v2
	s_nop 1
	v_cndmask_b32_e32 v126, v206, v126, vcc
	v_cmp_gt_u32_e32 vcc, s0, v0
	v_subrev_u32_e32 v0, 32, v0
	s_nop 0
	v_cndmask_b32_e32 v111, v206, v111, vcc
	v_cmp_gt_u32_e32 vcc, s0, v0
	s_nop 1
	v_cndmask_b32_e32 v127, v206, v127, vcc
